# v19 + MoE-up B-tile LDS-DMA de-waterfalled (uniform offset read once per iteration) so its light phases get the DMA-first interleave too
# speedup vs baseline: 1.0090x; 1.0029x over previous
;     __device__ __forceinline__ unsigned b_off(const Unit& u, const Gemm& g) const { return (unsigned)u.pn * (unsigned)(BM * 2) * (unsigned)g.K; }
;     __device__ __forceinline__ unsigned b_off(const Unit& u, const Gemm& g) const { return (unsigned)u.pn * (unsigned)(BM * 2) * (unsigned)g.K; }
; #define PG8_STAGE(bufoff, rs_, soff_, voff) do { _Pragma("unroll") for (int _i = 0; _i < 2; ++_i) \
;         __builtin_amdgcn_raw_ptr_buffer_load_lds(rs_, (LAS void*)(lds + (bufoff) + ldsw + _i * 8192), 16, (int)(voff)[_i], (int)(soff_), 0, 0); } while (0)
; #define PG8_LDA(dst, b, h) do { _Pragma("unroll") for (int m = 0; m < 4; ++m) dst[m] = PG8_LD2(lds + PG8_SA(b, h) + aoff + m * 2048); } while (0)
; #define PG8_BAR __builtin_amdgcn_s_barrier()
;     __device__ __forceinline__ unsigned b_off(const Unit& u, const Gemm& g) const {
;         int e = 0;
; #pragma unroll
;         for (int j = 1; j < 8; ++j) e += (u.pm >= ts[j]) ? 1 : 0;
;         return (unsigned)e * (unsigned)(wstride * 2) + (unsigned)u.pn * (unsigned)(BM * 2) * (unsigned)g.K;
;     }
; template <class Epi, class Sched, bool ALIGN_EPI = false, bool SP2 = false, bool FP8 = false>
; __device__ __forceinline__ void gemm_phase(LAS unsigned char* lds, const Gemm g, const Sched& S, const Epi& E, int wbase) {
;     ...
;             if constexpr (SP2) {
;             PG8_LDB(B0, 0, 0); PG8_LDB(B1, 0, 1); PG8_SCHED; PG8_LDA(At, 0, 0); PG8_STAGE(PG8_SA(1, 1), rAc, a1 + hstep, voffA);
;             PG8_WAIT_V(8); PG8_WAIT_L(0); PG8_BAR; PG8_MMA(0, 0, At, B0); PG8_MMA(0, 1, At, B1); PG8_BAR; PG8_SCHED;
;             PG8_LDA(At, 0, 1); PG8_STAGE(PG8_SB(0, 0), rB2, b2, voffB); PG8_STAGE(PG8_SB(0, 1), rB2, b2 + hstep, voffB); PG8_STAGE(PG8_SA(0, 0), rA2, a2, voffA);
;             PG8_WAIT_V(8); PG8_WAIT_L(0); PG8_BAR; PG8_MMA(1, 0, At, B0); PG8_MMA(1, 1, At, B1); PG8_BAR; PG8_SCHED;
;             PG8_LDB(B0, 1, 0); PG8_LDB(B1, 1, 1); PG8_SCHED; PG8_LDA(At, 1, 0); PG8_STAGE(PG8_SA(0, 1), rA2, a2 + hstep, voffA);
;             PG8_WAIT_V(8); PG8_WAIT_L(0); PG8_BAR; PG8_MMA(0, 0, At, B0); PG8_MMA(0, 1, At, B1); PG8_BAR; PG8_SCHED;
;             PG8_LDA(At, 1, 1); PG8_STAGE(PG8_SB(1, 0), rB2, b3, voffB); PG8_STAGE(PG8_SB(1, 1), rB2, b3 + hstep, voffB); PG8_STAGE(PG8_SA(1, 0), rA2, a3, voffA);
;             PG8_WAIT_V(8); PG8_WAIT_L(0); PG8_BAR; PG8_MMA(1, 0, At, B0); PG8_MMA(1, 1, At, B1); PG8_BAR; PG8_SCHED;
.LBB0_1348:
	v_add_u32_e32 v12, 0x10000, v199
	v_add_u32_e32 v28, 0x14000, v199
	ds_read_b128 v[0:3], v12
	ds_read_b128 v[4:7], v12 offset:1024
	ds_read_b128 v[8:11], v12 offset:2048
	ds_read_b128 v[12:15], v12 offset:3072
	ds_read_b128 v[16:19], v28
	ds_read_b128 v[20:23], v28 offset:1024
	ds_read_b128 v[24:27], v28 offset:2048
	ds_read_b128 v[28:31], v28 offset:3072
	s_add_i32 s6, s67, 0x80
	s_cmp_eq_u32 s65, s85
	s_cselect_b32 s54, s66, s6
	s_cselect_b64 vcc, -1, 0
	v_cndmask_b32_e32 v211, v210, v201, vcc
	s_or_b32 s78, s54, 0x80
	s_add_i32 s6, s41, s67
	s_mov_b32 m0, s76
	ds_read_b128 v[32:35], v200
	ds_read_b128 v[36:39], v200 offset:1024
	ds_read_b128 v[40:43], v200 offset:2048
	ds_read_b128 v[44:47], v200 offset:3072
	ds_read_b128 v[48:51], v200 offset:4096
	ds_read_b128 v[52:55], v200 offset:5120
	ds_read_b128 v[56:59], v200 offset:6144
	ds_read_b128 v[60:63], v200 offset:7168
	v_readfirstlane_b32 s55, v211
	s_add_i32 s20, s55, s41
	buffer_load_dwordx4 v192, s[36:39], s6 offen lds
	s_mov_b32 m0, s77
	s_nop 0
	buffer_load_dwordx4 v195, s[36:39], s6 offen lds
	s_waitcnt vmcnt(8)
	s_waitcnt lgkmcnt(0)
	s_barrier
	s_setprio 1
	v_mfma_f32_16x16x128_f8f6f4 v[184:187], v[0:7], v[32:39], v[184:187]
	v_mfma_f32_16x16x128_f8f6f4 v[188:191], v[8:15], v[32:39], v[188:191]
	v_mfma_f32_16x16x128_f8f6f4 v[168:171], v[0:7], v[40:47], v[168:171]
	v_mfma_f32_16x16x128_f8f6f4 v[172:175], v[8:15], v[40:47], v[172:175]
	v_mfma_f32_16x16x128_f8f6f4 v[152:155], v[0:7], v[48:55], v[152:155]
	v_mfma_f32_16x16x128_f8f6f4 v[156:159], v[8:15], v[48:55], v[156:159]
	v_mfma_f32_16x16x128_f8f6f4 v[136:139], v[0:7], v[56:63], v[136:139]
	v_mfma_f32_16x16x128_f8f6f4 v[140:143], v[8:15], v[56:63], v[140:143]
	v_mfma_f32_16x16x128_f8f6f4 v[176:179], v[16:23], v[32:39], v[176:179]
	v_mfma_f32_16x16x128_f8f6f4 v[180:183], v[24:31], v[32:39], v[180:183]
	v_mfma_f32_16x16x128_f8f6f4 v[160:163], v[16:23], v[40:47], v[160:163]
	v_mfma_f32_16x16x128_f8f6f4 v[164:167], v[24:31], v[40:47], v[164:167]
	v_mfma_f32_16x16x128_f8f6f4 v[144:147], v[16:23], v[48:55], v[144:147]
	v_mfma_f32_16x16x128_f8f6f4 v[148:151], v[24:31], v[48:55], v[148:151]
	v_mfma_f32_16x16x128_f8f6f4 v[128:131], v[16:23], v[56:63], v[128:131]
	v_mfma_f32_16x16x128_f8f6f4 v[132:135], v[24:31], v[56:63], v[132:135]
	s_setprio 0
	s_barrier
	s_mov_b32 s6, s38
	s_mov_b32 s7, s39
	s_mov_b32 m0, s43
	ds_read_b128 v[32:35], v200 offset:16384
	buffer_load_dwordx4 v194, s[4:7], s55 offen lds
	s_mov_b32 m0, s44
	ds_read_b128 v[36:39], v200 offset:17408
	buffer_load_dwordx4 v196, s[4:7], s55 offen lds
	s_mov_b32 m0, s45
	ds_read_b128 v[40:43], v200 offset:18432
	buffer_load_dwordx4 v194, s[4:7], s20 offen lds
	s_mov_b32 m0, s46
	ds_read_b128 v[44:47], v200 offset:19456
	buffer_load_dwordx4 v196, s[4:7], s20 offen lds
	s_mov_b32 m0, s42
	ds_read_b128 v[48:51], v200 offset:20480
	buffer_load_dwordx4 v192, s[36:39], s54 offen lds
	s_mov_b32 m0, s47
	ds_read_b128 v[52:55], v200 offset:21504
	buffer_load_dwordx4 v195, s[36:39], s54 offen lds
	ds_read_b128 v[56:59], v200 offset:22528
	ds_read_b128 v[60:63], v200 offset:23552
	s_waitcnt vmcnt(8)
	s_waitcnt lgkmcnt(0)
	s_barrier
	s_setprio 1
	v_mfma_f32_16x16x128_f8f6f4 v[120:123], v[0:7], v[32:39], v[120:123]
	v_mfma_f32_16x16x128_f8f6f4 v[124:127], v[8:15], v[32:39], v[124:127]
	v_mfma_f32_16x16x128_f8f6f4 v[104:107], v[0:7], v[40:47], v[104:107]
	v_mfma_f32_16x16x128_f8f6f4 v[108:111], v[8:15], v[40:47], v[108:111]
	v_mfma_f32_16x16x128_f8f6f4 v[88:91], v[0:7], v[48:55], v[88:91]
	v_mfma_f32_16x16x128_f8f6f4 v[92:95], v[8:15], v[48:55], v[92:95]
	v_mfma_f32_16x16x128_f8f6f4 v[72:75], v[0:7], v[56:63], v[72:75]
	v_mfma_f32_16x16x128_f8f6f4 v[76:79], v[8:15], v[56:63], v[76:79]
	v_mfma_f32_16x16x128_f8f6f4 v[112:115], v[16:23], v[32:39], v[112:115]
	v_mfma_f32_16x16x128_f8f6f4 v[116:119], v[24:31], v[32:39], v[116:119]
	v_mfma_f32_16x16x128_f8f6f4 v[96:99], v[16:23], v[40:47], v[96:99]
	v_mfma_f32_16x16x128_f8f6f4 v[100:103], v[24:31], v[40:47], v[100:103]
	v_mfma_f32_16x16x128_f8f6f4 v[80:83], v[16:23], v[48:55], v[80:83]
	v_mfma_f32_16x16x128_f8f6f4 v[84:87], v[24:31], v[48:55], v[84:87]
	v_mfma_f32_16x16x128_f8f6f4 v[68:71], v[16:23], v[56:63], v[68:71]
	v_mfma_f32_16x16x128_f8f6f4 v[64:67], v[24:31], v[56:63], v[64:67]
	s_setprio 0
	s_barrier
; #define PG8_STAGE(bufoff, rs_, soff_, voff) do { _Pragma("unroll") for (int _i = 0; _i < 2; ++_i) \
;         __builtin_amdgcn_raw_ptr_buffer_load_lds(rs_, (LAS void*)(lds + (bufoff) + ldsw + _i * 8192), 16, (int)(voff)[_i], (int)(soff_), 0, 0); } while (0)
; #define PG8_LDA(dst, b, h) do { _Pragma("unroll") for (int m = 0; m < 4; ++m) dst[m] = PG8_LD2(lds + PG8_SA(b, h) + aoff + m * 2048); } while (0)
; #define PG8_LDB(dst, b, h) do { _Pragma("unroll") for (int n = 0; n < 2; ++n) dst[n] = PG8_LD2(lds + PG8_SB(b, h) + boff + n * 2048); } while (0)
; #define PG8_WAIT_V(n) asm volatile("s_waitcnt vmcnt(" #n ")" ::: "memory")
; #define PG8_WAIT_L(n) asm volatile("s_waitcnt lgkmcnt(" #n ")" ::: "memory")
; #define PG8_BAR __builtin_amdgcn_s_barrier()
; #define PG8_SCHED __builtin_amdgcn_sched_barrier(0)
; template <class Epi, class Sched, bool ALIGN_EPI = false, bool SP2 = false, bool FP8 = false>
; __device__ __forceinline__ void gemm_phase(LAS unsigned char* lds, const Gemm g, const Sched& S, const Epi& E, int wbase) {
;     ...
;         for (int t = 0; t < nt; t += 2) {
;     ...
;             PG8_LDB(B0, 1, 0); PG8_LDB(B1, 1, 1); PG8_SCHED; PG8_LDA(At, 1, 0); PG8_STAGE(PG8_SA(0, 1), rA2, a2 + hstep, voffA);
;             PG8_WAIT_V(8); PG8_WAIT_L(0); PG8_BAR; PG8_MMA(0, 0, At, B0); PG8_MMA(0, 1, At, B1); PG8_BAR; PG8_SCHED;
;             PG8_LDA(At, 1, 1); PG8_STAGE(PG8_SB(1, 0), rB2, b3, voffB); PG8_STAGE(PG8_SB(1, 1), rB2, b3 + hstep, voffB); PG8_STAGE(PG8_SA(1, 0), rA2, a3, voffA);
;             PG8_WAIT_V(8); PG8_WAIT_L(0); PG8_BAR; PG8_MMA(1, 0, At, B0); PG8_MMA(1, 1, At, B1); PG8_BAR; PG8_SCHED;
	v_add_u32_e32 v12, 0x18000, v199
	v_add_u32_e32 v28, 0x1c000, v199
	ds_read_b128 v[0:3], v12
	ds_read_b128 v[4:7], v12 offset:1024
	ds_read_b128 v[8:11], v12 offset:2048
	ds_read_b128 v[12:15], v12 offset:3072
	ds_read_b128 v[16:19], v28
	ds_read_b128 v[20:23], v28 offset:1024
	ds_read_b128 v[24:27], v28 offset:2048
	ds_read_b128 v[28:31], v28 offset:3072
	s_add_i32 s54, s54, s41
	s_mov_b32 m0, s48
	ds_read_b128 v[32:35], v200 offset:32768
	ds_read_b128 v[36:39], v200 offset:33792
	ds_read_b128 v[40:43], v200 offset:34816
	ds_read_b128 v[44:47], v200 offset:35840
	ds_read_b128 v[48:51], v200 offset:36864
	ds_read_b128 v[52:55], v200 offset:37888
	ds_read_b128 v[56:59], v200 offset:38912
	ds_read_b128 v[60:63], v200 offset:39936
	buffer_load_dwordx4 v192, s[36:39], s54 offen lds
	s_mov_b32 m0, s52
	s_nop 0
	buffer_load_dwordx4 v195, s[36:39], s54 offen lds
	s_waitcnt vmcnt(8)
	s_waitcnt lgkmcnt(0)
	s_barrier
	s_setprio 1
	v_mfma_f32_16x16x128_f8f6f4 v[184:187], v[0:7], v[32:39], v[184:187]
	v_mfma_f32_16x16x128_f8f6f4 v[188:191], v[8:15], v[32:39], v[188:191]
	v_mfma_f32_16x16x128_f8f6f4 v[168:171], v[0:7], v[40:47], v[168:171]
	v_mfma_f32_16x16x128_f8f6f4 v[172:175], v[8:15], v[40:47], v[172:175]
	v_mfma_f32_16x16x128_f8f6f4 v[152:155], v[0:7], v[48:55], v[152:155]
	v_mfma_f32_16x16x128_f8f6f4 v[156:159], v[8:15], v[48:55], v[156:159]
	v_mfma_f32_16x16x128_f8f6f4 v[136:139], v[0:7], v[56:63], v[136:139]
	v_mfma_f32_16x16x128_f8f6f4 v[140:143], v[8:15], v[56:63], v[140:143]
	v_mfma_f32_16x16x128_f8f6f4 v[176:179], v[16:23], v[32:39], v[176:179]
	v_mfma_f32_16x16x128_f8f6f4 v[180:183], v[24:31], v[32:39], v[180:183]
	v_mfma_f32_16x16x128_f8f6f4 v[160:163], v[16:23], v[40:47], v[160:163]
	v_mfma_f32_16x16x128_f8f6f4 v[164:167], v[24:31], v[40:47], v[164:167]
	v_mfma_f32_16x16x128_f8f6f4 v[144:147], v[16:23], v[48:55], v[144:147]
	v_mfma_f32_16x16x128_f8f6f4 v[148:151], v[24:31], v[48:55], v[148:151]
	v_mfma_f32_16x16x128_f8f6f4 v[128:131], v[16:23], v[56:63], v[128:131]
	v_mfma_f32_16x16x128_f8f6f4 v[132:135], v[24:31], v[56:63], v[132:135]
	s_setprio 0
	s_barrier
	s_addk_i32 s55, 0x80
	s_addk_i32 s20, 0x80
	s_mov_b32 m0, s57
	ds_read_b128 v[32:35], v200 offset:49152
	buffer_load_dwordx4 v194, s[4:7], s55 offen lds
	s_mov_b32 m0, s58
	ds_read_b128 v[36:39], v200 offset:50176
	buffer_load_dwordx4 v196, s[4:7], s55 offen lds
	s_mov_b32 m0, s61
	ds_read_b128 v[40:43], v200 offset:51200
	buffer_load_dwordx4 v194, s[4:7], s20 offen lds
	s_mov_b32 m0, s62
	ds_read_b128 v[44:47], v200 offset:52224
	buffer_load_dwordx4 v196, s[4:7], s20 offen lds
	s_mov_b32 m0, s59
	ds_read_b128 v[48:51], v200 offset:53248
	buffer_load_dwordx4 v192, s[36:39], s78 offen lds
	s_mov_b32 m0, s60
	ds_read_b128 v[52:55], v200 offset:54272
	buffer_load_dwordx4 v195, s[36:39], s78 offen lds
	ds_read_b128 v[56:59], v200 offset:55296
	ds_read_b128 v[60:63], v200 offset:56320
	s_waitcnt vmcnt(8)
	s_waitcnt lgkmcnt(0)
	s_barrier
	s_setprio 1
	v_mfma_f32_16x16x128_f8f6f4 v[120:123], v[0:7], v[32:39], v[120:123]
	v_mfma_f32_16x16x128_f8f6f4 v[124:127], v[8:15], v[32:39], v[124:127]
	v_mfma_f32_16x16x128_f8f6f4 v[104:107], v[0:7], v[40:47], v[104:107]
	v_mfma_f32_16x16x128_f8f6f4 v[108:111], v[8:15], v[40:47], v[108:111]
	v_mfma_f32_16x16x128_f8f6f4 v[88:91], v[0:7], v[48:55], v[88:91]
	v_mfma_f32_16x16x128_f8f6f4 v[92:95], v[8:15], v[48:55], v[92:95]
	v_mfma_f32_16x16x128_f8f6f4 v[72:75], v[0:7], v[56:63], v[72:75]
	v_mfma_f32_16x16x128_f8f6f4 v[76:79], v[8:15], v[56:63], v[76:79]
	v_mfma_f32_16x16x128_f8f6f4 v[112:115], v[16:23], v[32:39], v[112:115]
	v_mfma_f32_16x16x128_f8f6f4 v[116:119], v[24:31], v[32:39], v[116:119]
	v_mfma_f32_16x16x128_f8f6f4 v[96:99], v[16:23], v[40:47], v[96:99]
	v_mfma_f32_16x16x128_f8f6f4 v[100:103], v[24:31], v[40:47], v[100:103]
	v_mfma_f32_16x16x128_f8f6f4 v[80:83], v[16:23], v[48:55], v[80:83]
	v_mfma_f32_16x16x128_f8f6f4 v[84:87], v[24:31], v[48:55], v[84:87]
	v_mfma_f32_16x16x128_f8f6f4 v[68:71], v[16:23], v[56:63], v[68:71]
	v_mfma_f32_16x16x128_f8f6f4 v[64:67], v[24:31], v[56:63], v[64:67]
	s_setprio 0
	s_barrier
	s_add_i32 s85, s85, 2
	s_addk_i32 s67, 0x100
	s_cmp_ge_i32 s85, s53
	v_add_u32_e32 v210, 0x100, v210
	s_cbranch_scc0 .LBB0_1348
	v_readlane_b32 s54, v255, 25
	v_readlane_b32 s55, v255, 26
	s_and_b64 vcc, exec, s[18:19]
	s_cbranch_vccnz .LBB0_1367
	s_branch .LBB0_1368
